# attention loops: row-sum adds spread behind their cvt, MFMA first in slot, counted lgkmcnt
# speedup vs baseline: 1.0099x; 1.0065x over previous
.LBB0_929:
	v_mfma_f32_32x32x16_bf16 v[114:129], v[98:101], v[130:133], 0
	s_lshl_b64 s[38:39], s[88:89], 13
	v_lshl_add_u64 v[102:103], v[214:215], 0, s[38:39]
	s_add_i32 m0, s34, 0x3000
	s_mul_i32 s34, s30, 0x5000
	global_load_lds_dwordx4 v[102:103], off
	s_add_i32 s34, s34, 0
	v_add_u32_e32 v208, s34, v231
	ds_read_b128 v[204:207], v208 offset:4608
	v_exp_f32_e32 v82, v82
	v_exp_f32_e32 v83, v83
	s_mul_i32 s35, s12, 0x5000
	s_mulk_i32 s33, 0x5000
	v_add_u32_e32 v235, s34, v233
	v_add_u32_e32 v210, s35, v232
	v_add_u32_e32 v209, s33, v234
	v_mfma_f32_32x32x16_bf16 v[98:113], v[98:101], v[170:173], 0
	v_cvt_pk_bf16_f32 v198, v82, v83
	v_add_f32_e32 v212, v82, v212
	v_add_f32_e32 v212, v83, v212
	v_exp_f32_e32 v200, v84
	v_exp_f32_e32 v201, v85
	v_mfma_f32_32x32x16_bf16 v[114:129], v[194:197], v[134:137], v[114:129]
	ds_read_b128 v[82:85], v208 offset:6656
	v_exp_f32_e32 v86, v86
	v_exp_f32_e32 v87, v87
	v_cvt_pk_bf16_f32 v199, v200, v201
	v_add_f32_e32 v212, v200, v212
	v_add_f32_e32 v212, v201, v212
	v_mfma_f32_32x32x16_bf16 v[98:113], v[194:197], v[138:141], v[98:113]
	v_exp_f32_e32 v195, v88
	v_exp_f32_e32 v196, v89
	v_cvt_pk_bf16_f32 v200, v86, v87
	v_add_f32_e32 v212, v86, v212
	v_add_f32_e32 v212, v87, v212
	s_waitcnt lgkmcnt(1)
	v_mfma_f32_32x32x16_bf16 v[114:129], v[204:207], v[146:149], v[114:129]
	ds_read_b128 v[86:89], v208 offset:8704
	v_cvt_pk_bf16_f32 v201, v195, v196
	v_add_f32_e32 v212, v195, v212
	v_add_f32_e32 v212, v196, v212
	v_mfma_f32_32x32x16_bf16 v[98:113], v[204:207], v[142:145], v[98:113]
	v_exp_f32_e32 v90, v90
	v_exp_f32_e32 v91, v91
	s_waitcnt lgkmcnt(1)
	v_mfma_f32_32x32x16_bf16 v[114:129], v[82:85], v[150:153], v[114:129]
	ds_read_b128 v[204:207], v208 offset:10752
	v_cvt_pk_bf16_f32 v194, v90, v91
	v_add_f32_e32 v212, v90, v212
	v_add_f32_e32 v212, v91, v212
	v_exp_f32_e32 v90, v92
	v_exp_f32_e32 v91, v93
	v_mfma_f32_32x32x16_bf16 v[98:113], v[82:85], v[154:157], v[98:113]
	v_cvt_pk_bf16_f32 v195, v90, v91
	v_add_f32_e32 v212, v90, v212
	v_add_f32_e32 v212, v91, v212
	v_exp_f32_e32 v90, v94
	v_exp_f32_e32 v91, v95
	s_waitcnt lgkmcnt(1)
	v_mfma_f32_32x32x16_bf16 v[114:129], v[86:89], v[162:165], v[114:129]
	ds_read_b128 v[82:85], v209 offset:16384
	v_exp_f32_e32 v95, v96
	v_exp_f32_e32 v96, v97
	v_cvt_pk_bf16_f32 v196, v90, v91
	v_add_f32_e32 v212, v90, v212
	v_add_f32_e32 v212, v91, v212
	v_mfma_f32_32x32x16_bf16 v[98:113], v[86:89], v[158:161], v[98:113]
	ds_read_b128 v[90:93], v209 offset:16896
	v_cvt_pk_bf16_f32 v197, v95, v96
	v_add_f32_e32 v212, v95, v212
	v_add_f32_e32 v212, v96, v212
	s_waitcnt lgkmcnt(2)
	v_mfma_f32_32x32x16_bf16 v[114:129], v[204:207], v[166:169], v[114:129]
	v_exp_f32_e32 v66, v66
	v_exp_f32_e32 v67, v67
	v_mfma_f32_32x32x16_bf16 v[98:113], v[204:207], v[174:177], v[98:113]
	v_exp_f32_e32 v87, v68
	v_exp_f32_e32 v88, v69
	v_cvt_pk_bf16_f32 v202, v66, v67
	v_add_f32_e32 v213, v66, v213
	v_add_f32_e32 v213, v67, v213
	s_waitcnt lgkmcnt(1)
	v_mfma_f32_32x32x16_bf16 v[18:33], v[82:85], v[178:181], v[18:33]
	ds_read_b128 v[66:69], v209 offset:18432
	v_exp_f32_e32 v70, v70
	v_exp_f32_e32 v71, v71
	v_cvt_pk_bf16_f32 v203, v87, v88
	v_add_f32_e32 v213, v87, v213
	v_add_f32_e32 v213, v88, v213
	s_waitcnt lgkmcnt(1)
	v_mfma_f32_32x32x16_bf16 v[34:49], v[90:93], v[178:181], v[34:49]
	ds_read_b128 v[86:89], v209 offset:18944
	v_cvt_pk_bf16_f32 v204, v70, v71
	v_add_f32_e32 v213, v70, v213
	v_add_f32_e32 v213, v71, v213
	v_exp_f32_e32 v70, v72
	v_exp_f32_e32 v71, v73
	v_mfma_f32_32x32x16_bf16 v[50:65], v[82:85], v[190:193], v[50:65]
	v_cvt_pk_bf16_f32 v205, v70, v71
	v_add_f32_e32 v213, v70, v213
	v_add_f32_e32 v213, v71, v213
	v_mfma_f32_32x32x16_bf16 v[2:17], v[90:93], v[190:193], v[2:17]
	v_exp_f32_e32 v74, v74
	v_exp_f32_e32 v75, v75
	s_waitcnt lgkmcnt(1)
	v_mfma_f32_32x32x16_bf16 v[18:33], v[66:69], v[182:185], v[18:33]
	ds_read_b128 v[70:73], v210
	v_cvt_pk_bf16_f32 v206, v74, v75
	v_add_f32_e32 v213, v74, v213
	v_add_f32_e32 v213, v75, v213
	v_exp_f32_e32 v74, v76
	v_exp_f32_e32 v75, v77
	s_waitcnt lgkmcnt(1)
	v_mfma_f32_32x32x16_bf16 v[34:49], v[86:89], v[182:185], v[34:49]
	v_cvt_pk_bf16_f32 v207, v74, v75
	v_add_f32_e32 v213, v74, v213
	v_add_f32_e32 v213, v75, v213
	v_exp_f32_e32 v74, v78
	v_exp_f32_e32 v75, v79
	v_mfma_f32_32x32x16_bf16 v[50:65], v[66:69], v[186:189], v[50:65]
	ds_read_b128 v[180:183], v210 offset:2048
	v_exp_f32_e32 v67, v80
	v_exp_f32_e32 v68, v81
	v_cvt_pk_bf16_f32 v208, v74, v75
	v_add_f32_e32 v213, v74, v213
	v_add_f32_e32 v213, v75, v213
	v_mfma_f32_32x32x16_bf16 v[2:17], v[86:89], v[186:189], v[2:17]
	v_cvt_pk_bf16_f32 v209, v67, v68
	v_add_f32_e32 v213, v67, v213
	v_add_f32_e32 v213, v68, v213
	s_waitcnt lgkmcnt(1)
	v_mfma_f32_32x32x16_bf16 v[82:97], v[70:73], v[130:133], 0
	ds_read_b128 v[184:187], v210 offset:4096
	v_exp_f32_e32 v114, v114
	v_exp_f32_e32 v115, v115
	v_mfma_f32_32x32x16_bf16 v[66:81], v[70:73], v[170:173], 0
	v_exp_f32_e32 v188, v116
	v_exp_f32_e32 v189, v117
	v_cvt_pk_bf16_f32 v178, v114, v115
	v_add_f32_e32 v212, v114, v212
	v_add_f32_e32 v212, v115, v212
	s_waitcnt lgkmcnt(1)
	v_mfma_f32_32x32x16_bf16 v[82:97], v[180:183], v[134:137], v[82:97]
	ds_read_b128 v[114:117], v210 offset:6144
	v_cvt_pk_bf16_f32 v179, v188, v189
	v_add_f32_e32 v212, v188, v212
	v_add_f32_e32 v212, v189, v212
	v_exp_f32_e32 v118, v118
	v_exp_f32_e32 v236, v119
	v_mfma_f32_32x32x16_bf16 v[66:81], v[180:183], v[138:141], v[66:81]
	v_cvt_pk_bf16_f32 v180, v118, v236
	v_add_f32_e32 v212, v118, v212
	v_add_f32_e32 v212, v236, v212
	v_exp_f32_e32 v240, v120
	v_exp_f32_e32 v242, v121
	s_waitcnt lgkmcnt(1)
	v_mfma_f32_32x32x16_bf16 v[82:97], v[184:187], v[146:149], v[82:97]
	ds_read_b128 v[118:121], v210 offset:8192
	v_cvt_pk_bf16_f32 v181, v240, v242
	v_add_f32_e32 v212, v240, v212
	v_add_f32_e32 v212, v242, v212
	v_mfma_f32_32x32x16_bf16 v[66:81], v[184:187], v[142:145], v[66:81]
	v_exp_f32_e32 v244, v122
	v_exp_f32_e32 v246, v123
	s_waitcnt lgkmcnt(1)
	v_mfma_f32_32x32x16_bf16 v[82:97], v[114:117], v[150:153], v[82:97]
	ds_read_b128 v[186:189], v210 offset:10240
	v_cvt_pk_bf16_f32 v182, v244, v246
	v_add_f32_e32 v212, v244, v212
	v_add_f32_e32 v212, v246, v212
	v_exp_f32_e32 v248, v124
	v_exp_f32_e32 v216, v125
	v_mfma_f32_32x32x16_bf16 v[66:81], v[114:117], v[154:157], v[66:81]
	v_cvt_pk_bf16_f32 v183, v248, v216
	v_add_f32_e32 v212, v248, v212
	v_add_f32_e32 v212, v216, v212
	v_exp_f32_e32 v218, v126
	v_exp_f32_e32 v220, v127
	s_waitcnt lgkmcnt(1)
	v_mfma_f32_32x32x16_bf16 v[82:97], v[118:121], v[162:165], v[82:97]
	ds_read_b128 v[114:117], v235 offset:12288
	v_cvt_pk_bf16_f32 v184, v218, v220
	v_add_f32_e32 v212, v218, v212
	v_add_f32_e32 v212, v220, v212
	v_exp_f32_e32 v222, v128
	v_exp_f32_e32 v224, v129
	v_mfma_f32_32x32x16_bf16 v[66:81], v[118:121], v[158:161], v[66:81]
	ds_read_b128 v[122:125], v235 offset:12800
	v_cvt_pk_bf16_f32 v185, v222, v224
	v_add_f32_e32 v212, v222, v212
	v_add_f32_e32 v212, v224, v212
	s_waitcnt lgkmcnt(2)
	v_mfma_f32_32x32x16_bf16 v[82:97], v[186:189], v[166:169], v[82:97]
	v_exp_f32_e32 v98, v98
	v_exp_f32_e32 v99, v99
	v_mfma_f32_32x32x16_bf16 v[66:81], v[186:189], v[174:177], v[66:81]
	v_cvt_pk_bf16_f32 v190, v98, v99
	v_add_f32_e32 v213, v98, v213
	v_add_f32_e32 v213, v99, v213
	v_exp_f32_e32 v98, v100
	v_exp_f32_e32 v99, v101
	s_waitcnt lgkmcnt(1)
	v_mfma_f32_32x32x16_bf16 v[18:33], v[114:117], v[198:201], v[18:33]
	ds_read_b128 v[118:121], v235 offset:14336
	v_cvt_pk_bf16_f32 v191, v98, v99
	v_add_f32_e32 v213, v98, v213
	v_add_f32_e32 v213, v99, v213
	v_exp_f32_e32 v98, v102
	v_exp_f32_e32 v237, v103
	s_waitcnt lgkmcnt(1)
	v_mfma_f32_32x32x16_bf16 v[34:49], v[122:125], v[198:201], v[34:49]
	ds_read_b128 v[126:129], v235 offset:14848
	v_cvt_pk_bf16_f32 v192, v98, v237
	v_add_f32_e32 v213, v98, v213
	v_add_f32_e32 v213, v237, v213
	v_exp_f32_e32 v241, v104
	v_exp_f32_e32 v243, v105
	v_mfma_f32_32x32x16_bf16 v[50:65], v[114:117], v[202:205], v[50:65]
	v_cvt_pk_bf16_f32 v193, v241, v243
	v_add_f32_e32 v213, v241, v213
	v_add_f32_e32 v213, v243, v213
	v_mfma_f32_32x32x16_bf16 v[2:17], v[122:125], v[202:205], v[2:17]
	v_exp_f32_e32 v245, v106
	v_exp_f32_e32 v247, v107
	s_waitcnt lgkmcnt(1)
	v_mfma_f32_32x32x16_bf16 v[18:33], v[118:121], v[194:197], v[18:33]
	ds_read_b128 v[98:101], v210 offset:512
	v_cvt_pk_bf16_f32 v186, v245, v247
	v_add_f32_e32 v213, v245, v213
	v_add_f32_e32 v213, v247, v213
	v_exp_f32_e32 v249, v108
	v_exp_f32_e32 v217, v109
	s_waitcnt lgkmcnt(1)
	v_mfma_f32_32x32x16_bf16 v[34:49], v[126:129], v[194:197], v[34:49]
	v_cvt_pk_bf16_f32 v187, v249, v217
	v_add_f32_e32 v213, v249, v213
	v_add_f32_e32 v213, v217, v213
	v_exp_f32_e32 v219, v110
	v_exp_f32_e32 v221, v111
	v_mfma_f32_32x32x16_bf16 v[50:65], v[118:121], v[206:209], v[50:65]
	ds_read_b128 v[194:197], v210 offset:2560
	v_cvt_pk_bf16_f32 v188, v219, v221
	v_add_f32_e32 v213, v219, v213
	v_add_f32_e32 v213, v221, v213
	v_exp_f32_e32 v223, v112
	v_exp_f32_e32 v225, v113
	v_mfma_f32_32x32x16_bf16 v[2:17], v[126:129], v[206:209], v[2:17]
	v_cvt_pk_bf16_f32 v189, v223, v225
	v_add_f32_e32 v213, v223, v213
	v_add_f32_e32 v213, v225, v213
	s_add_i32 s33, s13, 1
	s_waitcnt vmcnt(0)
	s_and_b32 s34, s33, 3
	s_add_i32 s31, s31, 1
	s_cmpk_eq_i32 s31, 0x104
	s_waitcnt vmcnt(0) lgkmcnt(0)
	s_barrier
	s_cbranch_scc1 .LBB0_931
	s_mov_b32 s33, s30
	s_mov_b32 s30, s12
	s_mov_b32 s12, s13
	s_mov_b32 s13, s34
	s_branch .LBB0_927

.LBB0_953:
	v_mfma_f32_32x32x16_bf16 v[114:129], v[98:101], v[130:133], 0
	s_min_i32 s28, s26, 0x101
	s_lshl_b32 s28, s28, 13
	s_add_i32 s88, s28, 0x4000
	s_lshl_b32 s28, s22, 14
	s_add_i32 s28, s21, s28
	v_lshl_add_u64 v[106:107], v[174:175], 0, s[88:89]
	s_mov_b32 m0, s28
	v_lshl_add_u32 v181, s27, 14, v0
	global_load_lds_dwordx4 v[106:107], off
	v_lshl_add_u64 v[106:107], v[176:177], 0, s[88:89]
	s_add_i32 m0, s28, 0x2000
	s_lshl_b32 s28, s25, 14
	global_load_lds_dwordx4 v[106:107], off
	ds_read_b128 v[190:193], v181 offset:12288
	v_add_u32_e32 v189, s28, v0
	v_lshl_add_u32 v210, s23, 14, v188
	v_exp_f32_e32 v194, v82
	v_exp_f32_e32 v196, v83
	v_exp_f32_e32 v198, v84
	v_exp_f32_e32 v200, v85
	v_mfma_f32_32x32x16_bf16 v[98:113], v[102:105], v[134:137], 0
	ds_read_b128 v[82:85], v181 offset:12800
	v_cvt_pk_bf16_f32 v170, v194, v196
	v_add_f32_e32 v232, v194, v232
	v_add_f32_e32 v232, v196, v232
	v_cvt_pk_bf16_f32 v171, v198, v200
	v_add_f32_e32 v232, v198, v232
	v_add_f32_e32 v232, v200, v232
	v_exp_f32_e32 v202, v86
	v_exp_f32_e32 v204, v87
	s_waitcnt lgkmcnt(3)
	v_mfma_f32_32x32x16_bf16 v[114:129], v[162:165], v[138:141], v[114:129]
	v_cvt_pk_bf16_f32 v172, v202, v204
	v_add_f32_e32 v232, v202, v232
	v_add_f32_e32 v232, v204, v232
	v_exp_f32_e32 v206, v88
	v_exp_f32_e32 v208, v89
	s_waitcnt lgkmcnt(2)
	v_mfma_f32_32x32x16_bf16 v[98:113], v[166:169], v[142:145], v[98:113]
	v_exp_f32_e32 v168, v92
	v_exp_f32_e32 v166, v93
	v_cvt_pk_bf16_f32 v173, v206, v208
	v_add_f32_e32 v232, v206, v232
	v_add_f32_e32 v232, v208, v232
	v_exp_f32_e32 v214, v90
	v_exp_f32_e32 v216, v91
	s_waitcnt lgkmcnt(1)
	v_mfma_f32_32x32x16_bf16 v[34:49], v[190:193], v[150:153], v[34:49]
	ds_read_b128 v[86:89], v181 offset:14336
	v_cvt_pk_bf16_f32 v162, v214, v216
	v_add_f32_e32 v232, v214, v232
	v_add_f32_e32 v232, v216, v232
	v_cvt_pk_bf16_f32 v163, v168, v166
	v_add_f32_e32 v232, v168, v232
	v_add_f32_e32 v232, v166, v232
	v_exp_f32_e32 v182, v94
	v_exp_f32_e32 v180, v95
	s_waitcnt lgkmcnt(1)
	v_mfma_f32_32x32x16_bf16 v[50:65], v[82:85], v[150:153], v[50:65]
	ds_read_b128 v[90:93], v181 offset:14848
	v_cvt_pk_bf16_f32 v164, v182, v180
	v_add_f32_e32 v232, v182, v232
	v_add_f32_e32 v232, v180, v232
	v_exp_f32_e32 v186, v96
	v_exp_f32_e32 v184, v97
	v_mfma_f32_32x32x16_bf16 v[2:17], v[190:193], v[158:161], v[2:17]
	v_cvt_pk_bf16_f32 v165, v186, v184
	v_add_f32_e32 v232, v186, v232
	v_add_f32_e32 v232, v184, v232
	v_exp_f32_e32 v195, v66
	v_exp_f32_e32 v197, v67
	v_exp_f32_e32 v199, v68
	v_exp_f32_e32 v201, v69
	v_mfma_f32_32x32x16_bf16 v[18:33], v[82:85], v[158:161], v[18:33]
	v_cvt_pk_bf16_f32 v158, v195, v197
	v_add_f32_e32 v233, v195, v233
	v_add_f32_e32 v233, v197, v233
	v_cvt_pk_bf16_f32 v159, v199, v201
	v_add_f32_e32 v233, v199, v233
	v_add_f32_e32 v233, v201, v233
	v_exp_f32_e32 v203, v70
	v_exp_f32_e32 v205, v71
	s_waitcnt lgkmcnt(1)
	v_mfma_f32_32x32x16_bf16 v[34:49], v[86:89], v[154:157], v[34:49]
	ds_read_b128 v[66:69], v210
	v_cvt_pk_bf16_f32 v160, v203, v205
	v_add_f32_e32 v233, v203, v233
	v_add_f32_e32 v233, v205, v233
	v_exp_f32_e32 v207, v72
	v_exp_f32_e32 v209, v73
	s_waitcnt lgkmcnt(1)
	v_mfma_f32_32x32x16_bf16 v[50:65], v[90:93], v[154:157], v[50:65]
	ds_read_b128 v[70:73], v210 offset:4096
	v_exp_f32_e32 v169, v76
	v_exp_f32_e32 v167, v77
	v_cvt_pk_bf16_f32 v161, v207, v209
	v_add_f32_e32 v233, v207, v233
	v_add_f32_e32 v233, v209, v233
	v_exp_f32_e32 v215, v74
	v_exp_f32_e32 v217, v75
	v_mfma_f32_32x32x16_bf16 v[2:17], v[86:89], v[146:149], v[2:17]
	ds_read_b128 v[152:155], v210 offset:2048
	v_cvt_pk_bf16_f32 v190, v215, v217
	v_add_f32_e32 v233, v215, v233
	v_add_f32_e32 v233, v217, v233
	v_cvt_pk_bf16_f32 v191, v169, v167
	v_add_f32_e32 v233, v169, v233
	v_add_f32_e32 v233, v167, v233
	v_exp_f32_e32 v183, v78
	v_exp_f32_e32 v181, v79
	v_mfma_f32_32x32x16_bf16 v[18:33], v[90:93], v[146:149], v[18:33]
	v_exp_f32_e32 v187, v80
	v_exp_f32_e32 v185, v81
	ds_read_b128 v[194:197], v210 offset:6144
	v_cvt_pk_bf16_f32 v192, v183, v181
	v_add_f32_e32 v233, v183, v233
	v_add_f32_e32 v233, v181, v233
	v_cvt_pk_bf16_f32 v193, v187, v185
	v_add_f32_e32 v233, v187, v233
	v_add_f32_e32 v233, v185, v233
	s_waitcnt lgkmcnt(3)
	v_mfma_f32_32x32x16_bf16 v[82:97], v[66:69], v[130:133], 0
	ds_read_b128 v[146:149], v189 offset:8192
	v_exp_f32_e32 v198, v114
	v_exp_f32_e32 v200, v115
	v_exp_f32_e32 v202, v116
	v_exp_f32_e32 v204, v117
	s_waitcnt lgkmcnt(3)
	v_mfma_f32_32x32x16_bf16 v[66:81], v[70:73], v[134:137], 0
	ds_read_b128 v[114:117], v189 offset:8704
	v_cvt_pk_bf16_f32 v150, v198, v200
	v_add_f32_e32 v232, v198, v232
	v_add_f32_e32 v232, v200, v232
	v_cvt_pk_bf16_f32 v151, v202, v204
	v_add_f32_e32 v232, v202, v232
	v_add_f32_e32 v232, v204, v232
	v_exp_f32_e32 v206, v118
	v_exp_f32_e32 v208, v119
	s_waitcnt lgkmcnt(3)
	v_mfma_f32_32x32x16_bf16 v[82:97], v[152:155], v[138:141], v[82:97]
	v_cvt_pk_bf16_f32 v152, v206, v208
	v_add_f32_e32 v232, v206, v232
	v_add_f32_e32 v232, v208, v232
	v_exp_f32_e32 v214, v120
	v_exp_f32_e32 v216, v121
	s_waitcnt lgkmcnt(2)
	v_mfma_f32_32x32x16_bf16 v[66:81], v[194:197], v[142:145], v[66:81]
	v_cvt_pk_bf16_f32 v153, v214, v216
	v_add_f32_e32 v232, v214, v232
	v_add_f32_e32 v232, v216, v232
	v_exp_f32_e32 v194, v122
	v_exp_f32_e32 v196, v123
	v_exp_f32_e32 v218, v124
	v_exp_f32_e32 v220, v125
	s_waitcnt lgkmcnt(1)
	v_mfma_f32_32x32x16_bf16 v[34:49], v[146:149], v[170:173], v[34:49]
	ds_read_b128 v[118:121], v189 offset:10240
	v_cvt_pk_bf16_f32 v154, v194, v196
	v_add_f32_e32 v232, v194, v232
	v_add_f32_e32 v232, v196, v232
	v_cvt_pk_bf16_f32 v155, v218, v220
	v_add_f32_e32 v232, v218, v232
	v_add_f32_e32 v232, v220, v232
	v_exp_f32_e32 v126, v126
	v_exp_f32_e32 v222, v127
	s_waitcnt lgkmcnt(1)
	v_mfma_f32_32x32x16_bf16 v[50:65], v[114:117], v[170:173], v[50:65]
	ds_read_b128 v[122:125], v189 offset:10752
	v_cvt_pk_bf16_f32 v156, v126, v222
	v_add_f32_e32 v232, v126, v232
	v_add_f32_e32 v232, v222, v232
	v_exp_f32_e32 v128, v128
	v_exp_f32_e32 v170, v129
	v_mfma_f32_32x32x16_bf16 v[2:17], v[146:149], v[158:161], v[2:17]
	v_cvt_pk_bf16_f32 v157, v128, v170
	v_add_f32_e32 v232, v128, v232
	v_add_f32_e32 v232, v170, v232
	v_exp_f32_e32 v199, v98
	v_exp_f32_e32 v201, v99
	v_exp_f32_e32 v203, v100
	v_exp_f32_e32 v205, v101
	v_mfma_f32_32x32x16_bf16 v[18:33], v[114:117], v[158:161], v[18:33]
	v_cvt_pk_bf16_f32 v158, v199, v201
	v_add_f32_e32 v233, v199, v233
	v_add_f32_e32 v233, v201, v233
	v_cvt_pk_bf16_f32 v159, v203, v205
	v_add_f32_e32 v233, v203, v233
	v_add_f32_e32 v233, v205, v233
	v_exp_f32_e32 v207, v102
	v_exp_f32_e32 v209, v103
	s_waitcnt lgkmcnt(1)
	v_mfma_f32_32x32x16_bf16 v[34:49], v[118:121], v[162:165], v[34:49]
	ds_read_b128 v[98:101], v210 offset:512
	v_cvt_pk_bf16_f32 v160, v207, v209
	v_add_f32_e32 v233, v207, v233
	v_add_f32_e32 v233, v209, v233
	v_exp_f32_e32 v215, v104
	v_exp_f32_e32 v217, v105
	s_waitcnt lgkmcnt(1)
	v_mfma_f32_32x32x16_bf16 v[50:65], v[122:125], v[162:165], v[50:65]
	ds_read_b128 v[102:105], v210 offset:4608
	v_cvt_pk_bf16_f32 v161, v215, v217
	v_add_f32_e32 v233, v215, v233
	v_add_f32_e32 v233, v217, v233
	v_exp_f32_e32 v195, v106
	v_exp_f32_e32 v197, v107
	v_exp_f32_e32 v219, v108
	v_exp_f32_e32 v221, v109
	v_mfma_f32_32x32x16_bf16 v[2:17], v[118:121], v[190:193], v[2:17]
	ds_read_b128 v[162:165], v210 offset:2560
	v_cvt_pk_bf16_f32 v146, v195, v197
	v_add_f32_e32 v233, v195, v233
	v_add_f32_e32 v233, v197, v233
	v_cvt_pk_bf16_f32 v147, v219, v221
	v_add_f32_e32 v233, v219, v233
	v_add_f32_e32 v233, v221, v233
	v_exp_f32_e32 v127, v110
	v_exp_f32_e32 v223, v111
	v_mfma_f32_32x32x16_bf16 v[18:33], v[122:125], v[190:193], v[18:33]
	v_exp_f32_e32 v129, v112
	ds_read_b128 v[166:169], v210 offset:6656
	v_exp_f32_e32 v171, v113
	v_cvt_pk_bf16_f32 v148, v127, v223
	v_add_f32_e32 v233, v127, v233
	v_add_f32_e32 v233, v223, v233
	v_cvt_pk_bf16_f32 v149, v129, v171
	v_add_f32_e32 v233, v129, v233
	v_add_f32_e32 v233, v171, v233
	s_add_i32 s27, s22, 1
	s_waitcnt vmcnt(0)
	s_and_b32 s28, s27, 3
	s_add_i32 s26, s26, 1
	s_cmpk_eq_i32 s26, 0x104
	s_mov_b32 s27, s25
	s_mov_b32 s25, s23
	s_mov_b32 s23, s22
	s_mov_b32 s22, s28
	s_waitcnt vmcnt(0) lgkmcnt(0)
	s_barrier
	s_cbranch_scc0 .LBB0_953
	v_mov_b32_e32 v178, v232
	v_mov_b32_e32 v179, v233
	ds_read_b128 v[66:69], v189 offset:12288
	ds_read_b128 v[70:73], v189 offset:12800
	v_mov_b32_e32 v0, v230
	s_waitcnt lgkmcnt(1)
	v_mfma_f32_32x32x16_bf16 v[34:49], v[66:69], v[150:153], v[34:49]
	s_waitcnt lgkmcnt(0)
	v_mfma_f32_32x32x16_bf16 v[50:65], v[70:73], v[150:153], v[50:65]
	v_mfma_f32_32x32x16_bf16 v[2:17], v[66:69], v[158:161], v[2:17]
	v_mfma_f32_32x32x16_bf16 v[18:33], v[70:73], v[158:161], v[18:33]
	ds_read_b128 v[68:71], v189 offset:14336
	ds_read_b128 v[72:75], v189 offset:14848
	v_mbcnt_lo_u32_b32 v76, -1, 0
	v_mbcnt_hi_u32_b32 v76, -1, v76
	v_mbcnt_lo_u32_b32 v77, -1, 0
	v_mbcnt_hi_u32_b32 v77, -1, v77
	global_load_dwordx2 v[66:67], v1, s[6:7]
	v_lshlrev_b32_e32 v77, 2, v77
	v_xor_b32_e32 v77, 0x80, v77
	v_lshlrev_b32_e32 v76, 2, v76
	ds_bpermute_b32 v77, v77, v179
	v_xor_b32_e32 v76, 0x80, v76
	ds_bpermute_b32 v76, v76, v178
	s_waitcnt lgkmcnt(3)
	v_mfma_f32_32x32x16_bf16 v[2:17], v[68:71], v[146:149], v[2:17]
	v_readfirstlane_b32 s21, v0
	s_ashr_i32 s21, s21, 1
	s_andn2_b32 s21, s21, 31
	s_cmpk_lt_i32 s21, 0x100
	s_waitcnt lgkmcnt(2)
	v_mfma_f32_32x32x16_bf16 v[18:33], v[72:75], v[146:149], v[18:33]
	v_mfma_f32_32x32x16_bf16 v[34:49], v[68:71], v[154:157], v[34:49]
	s_waitcnt lgkmcnt(1)
	v_add_f32_e32 v70, v179, v77
	v_mbcnt_lo_u32_b32 v68, -1, 0
	v_mbcnt_hi_u32_b32 v68, -1, v68
	v_rcp_f32_e32 v70, v70
	v_lshlrev_b32_e32 v69, 2, v68
	s_waitcnt lgkmcnt(0)
	v_add_f32_e32 v68, v178, v76
	v_rcp_f32_e32 v68, v68
	s_waitcnt vmcnt(0)
	v_mul_f32_e32 v66, v66, v70
	v_mfma_f32_32x32x16_bf16 v[50:65], v[72:75], v[154:157], v[50:65]
	v_mul_f32_e64 v2, v2, v66
	v_mul_f32_e64 v3, v3, v66
	v_mul_f32_e64 v18, v18, v66
	v_mul_f32_e64 v19, v19, v66
	v_mul_f32_e64 v4, v4, v66
	v_mul_f32_e64 v5, v5, v66
	v_pk_mul_f32 v[20:21], v[20:21], v[66:67] op_sel_hi:[1,0]
	v_pk_mul_f32 v[70:71], v[24:25], v[66:67] op_sel_hi:[1,0]
	v_pk_fma_f32 v[24:25], v[34:35], v[68:69], v[2:3] op_sel_hi:[1,0,1] neg_lo:[0,0,1] neg_hi:[0,0,1]
	v_pk_mul_f32 v[72:73], v[26:27], v[66:67] op_sel_hi:[1,0]
	s_nop 1
	v_pk_fma_f32 v[2:3], v[50:51], v[68:69], v[18:19] op_sel_hi:[1,0,1] neg_lo:[0,0,1] neg_hi:[0,0,1]
	v_pk_fma_f32 v[26:27], v[36:37], v[68:69], v[4:5] op_sel_hi:[1,0,1] neg_lo:[0,0,1] neg_hi:[0,0,1]
	v_pk_fma_f32 v[4:5], v[52:53], v[68:69], v[20:21] op_sel_hi:[1,0,1] neg_lo:[0,0,1] neg_hi:[0,0,1]
	v_pk_mul_f32 v[18:19], v[2:3], v[2:3]
	v_pk_mul_f32 v[6:7], v[6:7], v[66:67] op_sel_hi:[1,0]
	v_pk_mul_f32 v[22:23], v[22:23], v[66:67] op_sel_hi:[1,0]
	v_pk_mul_f32 v[36:37], v[4:5], v[4:5]
	v_pk_fma_f32 v[18:19], v[24:25], v[24:25], v[18:19]
	v_pk_mul_f32 v[74:75], v[28:29], v[66:67] op_sel_hi:[1,0]
	v_pk_fma_f32 v[28:29], v[38:39], v[68:69], v[6:7] op_sel_hi:[1,0,1] neg_lo:[0,0,1] neg_hi:[0,0,1]
	v_pk_fma_f32 v[6:7], v[54:55], v[68:69], v[22:23] op_sel_hi:[1,0,1] neg_lo:[0,0,1] neg_hi:[0,0,1]
	v_pk_fma_f32 v[36:37], v[26:27], v[26:27], v[36:37]
	v_add_f32_e32 v18, v18, v19
	v_pk_mul_f32 v[8:9], v[8:9], v[66:67] op_sel_hi:[1,0]
	v_pk_mul_f32 v[38:39], v[6:7], v[6:7]
	v_add_f32_e32 v18, v36, v18
	v_pk_mul_f32 v[76:77], v[30:31], v[66:67] op_sel_hi:[1,0]
	v_pk_fma_f32 v[30:31], v[40:41], v[68:69], v[8:9] op_sel_hi:[1,0,1] neg_lo:[0,0,1] neg_hi:[0,0,1]
	v_pk_fma_f32 v[8:9], v[56:57], v[68:69], v[70:71] op_sel_hi:[1,0,1] neg_lo:[0,0,1] neg_hi:[0,0,1]
	v_pk_fma_f32 v[38:39], v[28:29], v[28:29], v[38:39]
	v_add_f32_e32 v18, v37, v18
	v_pk_mul_f32 v[10:11], v[10:11], v[66:67] op_sel_hi:[1,0]
	v_pk_mul_f32 v[40:41], v[8:9], v[8:9]
	v_add_f32_e32 v18, v38, v18
	v_pk_mul_f32 v[78:79], v[32:33], v[66:67] op_sel_hi:[1,0]
	v_pk_fma_f32 v[32:33], v[42:43], v[68:69], v[10:11] op_sel_hi:[1,0,1] neg_lo:[0,0,1] neg_hi:[0,0,1]
	v_pk_fma_f32 v[10:11], v[58:59], v[68:69], v[72:73] op_sel_hi:[1,0,1] neg_lo:[0,0,1] neg_hi:[0,0,1]
	v_pk_fma_f32 v[40:41], v[30:31], v[30:31], v[40:41]
	v_add_f32_e32 v18, v39, v18
	v_pk_mul_f32 v[12:13], v[12:13], v[66:67] op_sel_hi:[1,0]
	v_pk_mul_f32 v[42:43], v[10:11], v[10:11]
	v_add_f32_e32 v18, v40, v18
	v_pk_fma_f32 v[34:35], v[44:45], v[68:69], v[12:13] op_sel_hi:[1,0,1] neg_lo:[0,0,1] neg_hi:[0,0,1]
	v_pk_fma_f32 v[12:13], v[60:61], v[68:69], v[74:75] op_sel_hi:[1,0,1] neg_lo:[0,0,1] neg_hi:[0,0,1]
	v_pk_fma_f32 v[42:43], v[32:33], v[32:33], v[42:43]
	v_add_f32_e32 v18, v41, v18
	v_pk_mul_f32 v[14:15], v[14:15], v[66:67] op_sel_hi:[1,0]
	v_pk_mul_f32 v[44:45], v[12:13], v[12:13]
	v_add_f32_e32 v18, v42, v18
	v_pk_fma_f32 v[20:21], v[46:47], v[68:69], v[14:15] op_sel_hi:[1,0,1] neg_lo:[0,0,1] neg_hi:[0,0,1]
	v_pk_fma_f32 v[14:15], v[62:63], v[68:69], v[76:77] op_sel_hi:[1,0,1] neg_lo:[0,0,1] neg_hi:[0,0,1]
	v_pk_fma_f32 v[44:45], v[34:35], v[34:35], v[44:45]
	v_add_f32_e32 v18, v43, v18
	v_pk_mul_f32 v[16:17], v[16:17], v[66:67] op_sel_hi:[1,0]
	v_pk_mul_f32 v[46:47], v[14:15], v[14:15]
	v_add_f32_e32 v18, v44, v18
	v_pk_fma_f32 v[22:23], v[48:49], v[68:69], v[16:17] op_sel_hi:[1,0,1] neg_lo:[0,0,1] neg_hi:[0,0,1]
	v_pk_fma_f32 v[16:17], v[64:65], v[68:69], v[78:79] op_sel_hi:[1,0,1] neg_lo:[0,0,1] neg_hi:[0,0,1]
	v_pk_fma_f32 v[46:47], v[20:21], v[20:21], v[46:47]
	v_add_f32_e32 v18, v45, v18
	v_pk_mul_f32 v[48:49], v[16:17], v[16:17]
	v_add_f32_e32 v18, v46, v18
	v_pk_fma_f32 v[48:49], v[22:23], v[22:23], v[48:49]
	v_add_f32_e32 v18, v47, v18
	v_add_f32_e32 v18, v48, v18
	v_add_f32_e32 v36, v49, v18
	v_xor_b32_e32 v18, 0x80, v69
	ds_bpermute_b32 v37, v18, v36
	s_cbranch_scc0 .LBB0_951
	s_waitcnt lgkmcnt(0)
	v_add_f32_e32 v36, v36, v37
	v_fmamk_f32 v36, v36, 0x3c800000, v224
	v_cmp_gt_f32_e32 vcc, s31, v36
	v_mul_f32_e32 v37, 0x4b800000, v36
	v_and_or_b32 v18, v0, 31, s21
	v_cndmask_b32_e32 v36, v36, v37, vcc
	v_rsq_f32_e32 v36, v36
	v_lshrrev_b32_e32 v0, 3, v0
	v_and_b32_e32 v0, 4, v0
	v_lshlrev_b32_e32 v41, 2, v0
	v_mul_f32_e32 v37, 0x45800000, v36
	v_cndmask_b32_e32 v36, v36, v37, vcc
	v_mul_f32_e32 v40, v67, v36
	global_load_dwordx4 v[36:39], v41, s[8:9] offset:128
	s_lshl_b64 s[10:11], s[10:11], 11
	s_add_u32 s10, s2, s10
	s_addc_u32 s11, s3, s11
	s_lshl_b32 s20, s20, 1
	s_add_u32 s10, s10, s20
	v_ashrrev_i32_e32 v19, 31, v18
	s_addc_u32 s11, s11, 0
	v_lshlrev_b64 v[18:19], 11, v[18:19]
	v_lshl_add_u64 v[18:19], s[10:11], 0, v[18:19]
	v_lshlrev_b32_e32 v0, 1, v0
	v_lshl_add_u64 v[18:19], v[18:19], 0, v[0:1]
	s_waitcnt vmcnt(0)
	v_pk_mul_f32 v[36:37], v[40:41], v[36:37] op_sel_hi:[0,1]
	v_pk_mul_f32 v[2:3], v[2:3], v[36:37]
	v_pk_mul_f32 v[36:37], v[40:41], v[38:39] op_sel_hi:[0,1]
	v_pk_mul_f32 v[4:5], v[4:5], v[36:37]
	global_load_dwordx4 v[36:39], v41, s[8:9] offset:160
	v_cvt_pk_bf16_f32 v2, v2, v3
	v_cvt_pk_bf16_f32 v3, v4, v5
	s_waitcnt vmcnt(0)
	v_pk_mul_f32 v[36:37], v[40:41], v[36:37] op_sel_hi:[0,1]
	v_pk_mul_f32 v[6:7], v[6:7], v[36:37]
	v_pk_mul_f32 v[36:37], v[40:41], v[38:39] op_sel_hi:[0,1]
	v_pk_mul_f32 v[8:9], v[8:9], v[36:37]
	global_load_dwordx4 v[36:39], v41, s[8:9] offset:192
	v_cvt_pk_bf16_f32 v4, v6, v7
	v_cvt_pk_bf16_f32 v5, v8, v9
	s_waitcnt vmcnt(0)
	v_pk_mul_f32 v[36:37], v[40:41], v[36:37] op_sel_hi:[0,1]
	v_pk_mul_f32 v[10:11], v[10:11], v[36:37]
	v_pk_mul_f32 v[36:37], v[40:41], v[38:39] op_sel_hi:[0,1]
	v_pk_mul_f32 v[12:13], v[12:13], v[36:37]
	global_load_dwordx4 v[36:39], v41, s[8:9] offset:224
	s_waitcnt vmcnt(0)
	v_pk_mul_f32 v[36:37], v[40:41], v[36:37] op_sel_hi:[0,1]
	v_pk_mul_f32 v[14:15], v[14:15], v[36:37]
	v_pk_mul_f32 v[36:37], v[40:41], v[38:39] op_sel_hi:[0,1]
	v_pk_mul_f32 v[16:17], v[16:17], v[36:37]
	global_load_dwordx4 v[36:39], v41, s[8:9]
	s_waitcnt vmcnt(0)
	v_pk_mul_f32 v[36:37], v[40:41], v[36:37] op_sel_hi:[0,1]
	v_pk_mul_f32 v[24:25], v[24:25], v[36:37]
	v_pk_mul_f32 v[36:37], v[40:41], v[38:39] op_sel_hi:[0,1]
	v_pk_mul_f32 v[26:27], v[26:27], v[36:37]
	global_load_dwordx4 v[36:39], v41, s[8:9] offset:32
	v_cvt_pk_bf16_f32 v24, v24, v25
	v_cvt_pk_bf16_f32 v25, v26, v27
	s_waitcnt vmcnt(0)
	v_pk_mul_f32 v[36:37], v[40:41], v[36:37] op_sel_hi:[0,1]
	v_pk_mul_f32 v[28:29], v[28:29], v[36:37]
	v_pk_mul_f32 v[36:37], v[40:41], v[38:39] op_sel_hi:[0,1]
	v_pk_mul_f32 v[30:31], v[30:31], v[36:37]
	global_load_dwordx4 v[36:39], v41, s[8:9] offset:64
	s_waitcnt vmcnt(0)
	v_pk_mul_f32 v[36:37], v[40:41], v[36:37] op_sel_hi:[0,1]
	v_pk_mul_f32 v[32:33], v[32:33], v[36:37]
	v_pk_mul_f32 v[36:37], v[40:41], v[38:39] op_sel_hi:[0,1]
	v_pk_mul_f32 v[34:35], v[34:35], v[36:37]
	global_load_dwordx4 v[36:39], v41, s[8:9] offset:96
	s_nop 0
	global_store_dwordx2 v[18:19], v[24:25], off offset:1024
	global_store_dwordx2 v[18:19], v[2:3], off offset:1088
	v_cvt_pk_bf16_f32 v2, v28, v29
	v_cvt_pk_bf16_f32 v3, v30, v31
	global_store_dwordx2 v[18:19], v[2:3], off offset:1040
	global_store_dwordx2 v[18:19], v[4:5], off offset:1104
	v_cvt_pk_bf16_f32 v2, v32, v33
	v_cvt_pk_bf16_f32 v3, v34, v35
	v_cvt_pk_bf16_f32 v4, v10, v11
	v_cvt_pk_bf16_f32 v5, v12, v13
	global_store_dwordx2 v[18:19], v[2:3], off offset:1056
	global_store_dwordx2 v[18:19], v[4:5], off offset:1120
	v_cvt_pk_bf16_f32 v4, v14, v15
	v_cvt_pk_bf16_f32 v5, v16, v17
	s_waitcnt vmcnt(6)
	v_pk_mul_f32 v[36:37], v[40:41], v[36:37] op_sel_hi:[0,1]
	v_pk_mul_f32 v[20:21], v[20:21], v[36:37]
	v_pk_mul_f32 v[36:37], v[40:41], v[38:39] op_sel_hi:[0,1]
	v_pk_mul_f32 v[22:23], v[22:23], v[36:37]
	v_cvt_pk_bf16_f32 v2, v20, v21
	v_cvt_pk_bf16_f32 v3, v22, v23
	global_store_dwordx2 v[18:19], v[2:3], off offset:1072
	global_store_dwordx2 v[18:19], v[4:5], off offset:1136
	s_branch .LBB0_951

.LBB0_967:
	v_mfma_f32_32x32x16_bf16 v[114:129], v[98:101], v[130:133], 0
	s_min_i32 s23, s21, 0x101
	s_lshl_b32 s23, s23, 13
	s_add_i32 s88, s23, 0x4000
	s_lshl_b32 s23, s19, 14
	s_add_i32 s23, s16, s23
	v_lshl_add_u64 v[102:103], v[194:195], 0, s[88:89]
	s_mov_b32 m0, s23
	v_lshl_add_u32 v211, s17, 14, v215
	global_load_lds_dwordx4 v[102:103], off
	v_lshl_add_u64 v[102:103], v[196:197], 0, s[88:89]
	s_add_i32 m0, s23, 0x2000
	s_lshl_b32 s23, s20, 14
	global_load_lds_dwordx4 v[102:103], off
	s_add_i32 s23, s23, 0
	v_add_u32_e32 v183, s23, v214
	ds_read_b128 v[188:191], v183 offset:4608
	v_add_u32_e32 v232, s23, v0
	v_lshl_add_u32 v192, s22, 14, v231
	v_exp_f32_e32 v216, v82
	v_exp_f32_e32 v218, v83
	v_mfma_f32_32x32x16_bf16 v[98:113], v[98:101], v[134:137], 0
	v_cvt_pk_bf16_f32 v182, v216, v218
	v_add_f32_e32 v233, v216, v233
	v_add_f32_e32 v233, v218, v233
	v_exp_f32_e32 v220, v84
	v_exp_f32_e32 v222, v85
	v_mfma_f32_32x32x16_bf16 v[114:129], v[178:181], v[138:141], v[114:129]
	ds_read_b128 v[82:85], v183 offset:6656
	v_cvt_pk_bf16_f32 v183, v220, v222
	v_add_f32_e32 v233, v220, v233
	v_add_f32_e32 v233, v222, v233
	v_exp_f32_e32 v224, v86
	v_exp_f32_e32 v238, v87
	v_mfma_f32_32x32x16_bf16 v[98:113], v[178:181], v[142:145], v[98:113]
	v_cvt_pk_bf16_f32 v184, v224, v238
	v_add_f32_e32 v233, v224, v233
	v_add_f32_e32 v233, v238, v233
	v_exp_f32_e32 v240, v88
	v_exp_f32_e32 v242, v89
	s_waitcnt lgkmcnt(1)
	v_mfma_f32_32x32x16_bf16 v[114:129], v[188:191], v[146:149], v[114:129]
	ds_read_b128 v[86:89], v192 offset:12288
	v_cvt_pk_bf16_f32 v185, v240, v242
	v_add_f32_e32 v233, v240, v233
	v_add_f32_e32 v233, v242, v233
	v_exp_f32_e32 v244, v90
	v_exp_f32_e32 v246, v91
	v_mfma_f32_32x32x16_bf16 v[98:113], v[188:191], v[150:153], v[98:113]
	ds_read_b128 v[234:237], v192 offset:12800
	v_cvt_pk_bf16_f32 v178, v244, v246
	v_add_f32_e32 v233, v244, v233
	v_add_f32_e32 v233, v246, v233
	v_exp_f32_e32 v200, v92
	v_exp_f32_e32 v198, v93
	s_waitcnt lgkmcnt(2)
	v_mfma_f32_32x32x16_bf16 v[114:129], v[82:85], v[154:157], v[114:129]
	s_nop 0
	v_cvt_pk_bf16_f32 v179, v200, v198
	v_add_f32_e32 v233, v200, v233
	v_add_f32_e32 v233, v198, v233
	v_exp_f32_e32 v204, v94
	v_exp_f32_e32 v202, v95
	v_mfma_f32_32x32x16_bf16 v[98:113], v[82:85], v[158:161], v[98:113]
	v_cvt_pk_bf16_f32 v180, v204, v202
	v_add_f32_e32 v233, v204, v233
	v_add_f32_e32 v233, v202, v233
	v_exp_f32_e32 v208, v96
	v_exp_f32_e32 v206, v97
	s_waitcnt lgkmcnt(1)
	v_mfma_f32_32x32x16_bf16 v[2:17], v[86:89], v[162:165], v[2:17]
	ds_read_b128 v[82:85], v192 offset:14336
	v_cvt_pk_bf16_f32 v181, v208, v206
	v_add_f32_e32 v233, v208, v233
	v_add_f32_e32 v233, v206, v233
	v_exp_f32_e32 v217, v66
	v_exp_f32_e32 v219, v67
	s_waitcnt lgkmcnt(1)
	v_mfma_f32_32x32x16_bf16 v[18:33], v[234:237], v[162:165], v[18:33]
	ds_read_b128 v[90:93], v192 offset:14848
	v_cvt_pk_bf16_f32 v190, v217, v219
	v_add_f32_e32 v227, v217, v227
	v_add_f32_e32 v227, v219, v227
	v_exp_f32_e32 v221, v68
	v_exp_f32_e32 v223, v69
	v_mfma_f32_32x32x16_bf16 v[34:49], v[86:89], v[174:177], v[34:49]
	v_cvt_pk_bf16_f32 v191, v221, v223
	v_add_f32_e32 v227, v221, v227
	v_add_f32_e32 v227, v223, v227
	v_exp_f32_e32 v225, v70
	v_exp_f32_e32 v239, v71
	v_mfma_f32_32x32x16_bf16 v[50:65], v[234:237], v[174:177], v[50:65]
	v_cvt_pk_bf16_f32 v192, v225, v239
	v_add_f32_e32 v227, v225, v227
	v_add_f32_e32 v227, v239, v227
	v_exp_f32_e32 v241, v72
	v_exp_f32_e32 v243, v73
	s_waitcnt lgkmcnt(1)
	v_mfma_f32_32x32x16_bf16 v[2:17], v[82:85], v[166:169], v[2:17]
	ds_read_b128 v[66:69], v211
	v_cvt_pk_bf16_f32 v193, v241, v243
	v_add_f32_e32 v227, v241, v227
	v_add_f32_e32 v227, v243, v227
	v_exp_f32_e32 v245, v74
	v_exp_f32_e32 v247, v75
	s_waitcnt lgkmcnt(1)
	v_mfma_f32_32x32x16_bf16 v[18:33], v[90:93], v[166:169], v[18:33]
	v_cvt_pk_bf16_f32 v186, v245, v247
	v_add_f32_e32 v227, v245, v227
	v_add_f32_e32 v227, v247, v227
	v_exp_f32_e32 v201, v76
	v_exp_f32_e32 v199, v77
	v_mfma_f32_32x32x16_bf16 v[34:49], v[82:85], v[170:173], v[34:49]
	ds_read_b128 v[164:167], v211 offset:2048
	v_cvt_pk_bf16_f32 v187, v201, v199
	v_add_f32_e32 v227, v201, v227
	v_add_f32_e32 v227, v199, v227
	v_exp_f32_e32 v205, v78
	v_exp_f32_e32 v203, v79
	v_mfma_f32_32x32x16_bf16 v[50:65], v[90:93], v[170:173], v[50:65]
	v_exp_f32_e32 v209, v80
	v_exp_f32_e32 v207, v81
	v_cvt_pk_bf16_f32 v188, v205, v203
	v_add_f32_e32 v227, v205, v227
	v_add_f32_e32 v227, v203, v227
	v_cvt_pk_bf16_f32 v189, v209, v207
	v_add_f32_e32 v227, v209, v227
	v_add_f32_e32 v227, v207, v227
	s_waitcnt lgkmcnt(1)
	v_mfma_f32_32x32x16_bf16 v[82:97], v[66:69], v[130:133], 0
	ds_read_b128 v[168:171], v211 offset:4096
	v_exp_f32_e32 v172, v114
	v_exp_f32_e32 v216, v115
	v_mfma_f32_32x32x16_bf16 v[66:81], v[66:69], v[134:137], 0
	v_cvt_pk_bf16_f32 v162, v172, v216
	v_add_f32_e32 v233, v172, v233
	v_add_f32_e32 v233, v216, v233
	v_exp_f32_e32 v218, v116
	v_exp_f32_e32 v220, v117
	s_waitcnt lgkmcnt(1)
	v_mfma_f32_32x32x16_bf16 v[82:97], v[164:167], v[138:141], v[82:97]
	ds_read_b128 v[114:117], v211 offset:6144
	v_cvt_pk_bf16_f32 v163, v218, v220
	v_add_f32_e32 v233, v218, v233
	v_add_f32_e32 v233, v220, v233
	v_exp_f32_e32 v222, v118
	v_exp_f32_e32 v224, v119
	v_mfma_f32_32x32x16_bf16 v[66:81], v[164:167], v[142:145], v[66:81]
	v_cvt_pk_bf16_f32 v164, v222, v224
	v_add_f32_e32 v233, v222, v233
	v_add_f32_e32 v233, v224, v233
	v_exp_f32_e32 v238, v120
	v_exp_f32_e32 v240, v121
	s_waitcnt lgkmcnt(1)
	v_mfma_f32_32x32x16_bf16 v[82:97], v[168:171], v[146:149], v[82:97]
	ds_read_b128 v[118:121], v232 offset:8192
	v_cvt_pk_bf16_f32 v165, v238, v240
	v_add_f32_e32 v233, v238, v233
	v_add_f32_e32 v233, v240, v233
	v_exp_f32_e32 v242, v122
	v_exp_f32_e32 v244, v123
	v_mfma_f32_32x32x16_bf16 v[66:81], v[168:171], v[150:153], v[66:81]
	ds_read_b128 v[234:237], v232 offset:8704
	v_cvt_pk_bf16_f32 v166, v242, v244
	v_add_f32_e32 v233, v242, v233
	v_add_f32_e32 v233, v244, v233
	v_exp_f32_e32 v246, v124
	v_exp_f32_e32 v248, v125
	s_waitcnt lgkmcnt(2)
	v_mfma_f32_32x32x16_bf16 v[82:97], v[114:117], v[154:157], v[82:97]
	v_cvt_pk_bf16_f32 v167, v246, v248
	v_add_f32_e32 v233, v246, v233
	v_add_f32_e32 v233, v248, v233
	v_exp_f32_e32 v126, v126
	v_exp_f32_e32 v212, v127
	v_mfma_f32_32x32x16_bf16 v[66:81], v[114:117], v[158:161], v[66:81]
	v_cvt_pk_bf16_f32 v168, v126, v212
	v_add_f32_e32 v233, v126, v233
	v_add_f32_e32 v233, v212, v233
	v_exp_f32_e32 v128, v128
	v_exp_f32_e32 v210, v129
	s_waitcnt lgkmcnt(1)
	v_mfma_f32_32x32x16_bf16 v[2:17], v[118:121], v[182:185], v[2:17]
	ds_read_b128 v[114:117], v232 offset:10240
	v_exp_f32_e32 v173, v98
	v_cvt_pk_bf16_f32 v169, v128, v210
	v_add_f32_e32 v233, v128, v233
	v_add_f32_e32 v233, v210, v233
	v_exp_f32_e32 v217, v99
	s_waitcnt lgkmcnt(1)
	v_mfma_f32_32x32x16_bf16 v[18:33], v[234:237], v[182:185], v[18:33]
	ds_read_b128 v[122:125], v232 offset:10752
	v_cvt_pk_bf16_f32 v174, v173, v217
	v_add_f32_e32 v227, v173, v227
	v_add_f32_e32 v227, v217, v227
	v_exp_f32_e32 v219, v100
	v_exp_f32_e32 v221, v101
	v_mfma_f32_32x32x16_bf16 v[34:49], v[118:121], v[190:193], v[34:49]
	v_cvt_pk_bf16_f32 v175, v219, v221
	v_add_f32_e32 v227, v219, v227
	v_add_f32_e32 v227, v221, v227
	v_exp_f32_e32 v223, v102
	v_exp_f32_e32 v225, v103
	v_mfma_f32_32x32x16_bf16 v[50:65], v[234:237], v[190:193], v[50:65]
	v_cvt_pk_bf16_f32 v176, v223, v225
	v_add_f32_e32 v227, v223, v227
	v_add_f32_e32 v227, v225, v227
	v_exp_f32_e32 v239, v104
	v_exp_f32_e32 v241, v105
	s_waitcnt lgkmcnt(1)
	v_mfma_f32_32x32x16_bf16 v[2:17], v[114:117], v[178:181], v[2:17]
	ds_read_b128 v[98:101], v211 offset:512
	v_cvt_pk_bf16_f32 v177, v239, v241
	v_add_f32_e32 v227, v239, v227
	v_add_f32_e32 v227, v241, v227
	v_exp_f32_e32 v243, v106
	v_exp_f32_e32 v245, v107
	s_waitcnt lgkmcnt(1)
	v_mfma_f32_32x32x16_bf16 v[18:33], v[122:125], v[178:181], v[18:33]
	v_cvt_pk_bf16_f32 v170, v243, v245
	v_add_f32_e32 v227, v243, v227
	v_add_f32_e32 v227, v245, v227
	v_exp_f32_e32 v247, v108
	v_exp_f32_e32 v249, v109
	v_mfma_f32_32x32x16_bf16 v[34:49], v[114:117], v[186:189], v[34:49]
	ds_read_b128 v[178:181], v211 offset:2560
	v_cvt_pk_bf16_f32 v171, v247, v249
	v_add_f32_e32 v227, v247, v227
	v_add_f32_e32 v227, v249, v227
	v_exp_f32_e32 v127, v110
	v_exp_f32_e32 v213, v111
	v_mfma_f32_32x32x16_bf16 v[50:65], v[122:125], v[186:189], v[50:65]
	v_exp_f32_e32 v129, v112
	v_exp_f32_e32 v211, v113
	v_cvt_pk_bf16_f32 v172, v127, v213
	v_add_f32_e32 v227, v127, v227
	v_add_f32_e32 v227, v213, v227
	v_cvt_pk_bf16_f32 v173, v129, v211
	v_add_f32_e32 v227, v129, v227
	v_add_f32_e32 v227, v211, v227
	s_add_i32 s22, s19, 1
	s_waitcnt vmcnt(0)
	s_and_b32 s23, s22, 3
	s_add_i32 s21, s21, 1
	s_cmpk_eq_i32 s21, 0x104
	s_mov_b32 s22, s20
	s_mov_b32 s20, s17
	s_mov_b32 s17, s19
	s_mov_b32 s19, s23
	s_waitcnt vmcnt(0) lgkmcnt(0)
	s_barrier
	s_cbranch_scc0 .LBB0_967
	v_mov_b32_e32 v186, v233
	v_mov_b32_e32 v187, v227
	v_mov_b32_e32 v227, 0x7c
	ds_read_b128 v[66:69], v232 offset:12288
	ds_read_b128 v[70:73], v232 offset:12800
	v_mov_b32_e32 v0, v230
	s_waitcnt lgkmcnt(1)
	v_mfma_f32_32x32x16_bf16 v[2:17], v[66:69], v[162:165], v[2:17]
	s_waitcnt lgkmcnt(0)
	v_mfma_f32_32x32x16_bf16 v[18:33], v[70:73], v[162:165], v[18:33]
	v_mfma_f32_32x32x16_bf16 v[34:49], v[66:69], v[174:177], v[34:49]
	v_mfma_f32_32x32x16_bf16 v[50:65], v[70:73], v[174:177], v[50:65]
	ds_read_b128 v[66:69], v232 offset:14336
	ds_read_b128 v[70:73], v232 offset:14848
	s_nop 0
	v_readfirstlane_b32 s16, v0
	s_ashr_i32 s16, s16, 1
	s_andn2_b32 s16, s16, 31
	s_cmpk_lt_i32 s16, 0x100
	s_waitcnt lgkmcnt(1)
	v_mfma_f32_32x32x16_bf16 v[2:17], v[66:69], v[166:169], v[2:17]
	s_waitcnt lgkmcnt(0)
	v_mfma_f32_32x32x16_bf16 v[18:33], v[70:73], v[166:169], v[18:33]
	v_mfma_f32_32x32x16_bf16 v[34:49], v[66:69], v[170:173], v[34:49]
	v_mbcnt_lo_u32_b32 v66, -1, 0
	v_mbcnt_hi_u32_b32 v66, -1, v66
	v_mbcnt_lo_u32_b32 v67, -1, 0
	v_mbcnt_hi_u32_b32 v67, -1, v67
	s_nop 0
	v_lshlrev_b32_e32 v66, 2, v66
	v_lshlrev_b32_e32 v67, 2, v67
	v_xor_b32_e32 v66, 0x80, v66
	v_xor_b32_e32 v67, 0x80, v67
	v_mfma_f32_32x32x16_bf16 v[50:65], v[70:73], v[170:173], v[50:65]
	ds_bpermute_b32 v66, v66, v186
	ds_bpermute_b32 v67, v67, v187
	s_cbranch_scc0 .LBB0_965
	s_lshl_b64 s[6:7], s[6:7], 11
	s_waitcnt lgkmcnt(1)
	v_add_f32_e32 v66, v186, v66
	s_add_u32 s6, s2, s6
	v_rcp_f32_e32 v66, v66
	s_addc_u32 s7, s3, s7
	s_lshl_b32 s15, s15, 1
	v_and_or_b32 v68, v0, 31, s16
	s_add_u32 s6, s6, s15
	v_ashrrev_i32_e32 v69, 31, v68
	s_addc_u32 s7, s7, 0
	s_waitcnt lgkmcnt(0)
	v_add_f32_e32 v67, v187, v67
	v_lshlrev_b64 v[68:69], 11, v[68:69]
	v_lshrrev_b32_e32 v0, 2, v0
	v_rcp_f32_e32 v70, v67
	v_lshl_add_u64 v[68:69], s[6:7], 0, v[68:69]
	v_pk_mul_f32 v[2:3], v[2:3], v[66:67] op_sel_hi:[1,0]
	v_pk_mul_f32 v[4:5], v[4:5], v[66:67] op_sel_hi:[1,0]
	v_and_b32_e32 v0, 8, v0
	v_pk_mul_f32 v[18:19], v[18:19], v[66:67] op_sel_hi:[1,0]
	v_pk_mul_f32 v[20:21], v[20:21], v[66:67] op_sel_hi:[1,0]
	v_pk_mul_f32 v[22:23], v[22:23], v[66:67] op_sel_hi:[1,0]
	v_pk_mul_f32 v[24:25], v[24:25], v[66:67] op_sel_hi:[1,0]
	v_pk_mul_f32 v[26:27], v[26:27], v[66:67] op_sel_hi:[1,0]
	v_pk_mul_f32 v[28:29], v[28:29], v[66:67] op_sel_hi:[1,0]
	v_pk_mul_f32 v[30:31], v[30:31], v[66:67] op_sel_hi:[1,0]
	v_pk_mul_f32 v[32:33], v[32:33], v[66:67] op_sel_hi:[1,0]
	v_pk_mul_f32 v[6:7], v[6:7], v[66:67] op_sel_hi:[1,0]
	v_pk_mul_f32 v[8:9], v[8:9], v[66:67] op_sel_hi:[1,0]
	v_pk_mul_f32 v[10:11], v[10:11], v[66:67] op_sel_hi:[1,0]
	v_pk_mul_f32 v[12:13], v[12:13], v[66:67] op_sel_hi:[1,0]
	v_pk_mul_f32 v[14:15], v[14:15], v[66:67] op_sel_hi:[1,0]
	v_pk_mul_f32 v[16:17], v[16:17], v[66:67] op_sel_hi:[1,0]
	v_lshl_add_u64 v[66:67], v[68:69], 0, v[0:1]
	v_cvt_pk_bf16_f32 v2, v2, v3
	v_cvt_pk_bf16_f32 v3, v4, v5
	v_cvt_pk_bf16_f32 v4, v18, v19
	v_cvt_pk_bf16_f32 v5, v20, v21
	global_store_dwordx2 v[66:67], v[2:3], off offset:1536
	global_store_dwordx2 v[66:67], v[4:5], off offset:1600
	v_cvt_pk_bf16_f32 v2, v6, v7
	v_cvt_pk_bf16_f32 v3, v8, v9
	v_cvt_pk_bf16_f32 v4, v22, v23
	v_cvt_pk_bf16_f32 v5, v24, v25
	global_store_dwordx2 v[66:67], v[2:3], off offset:1552
	global_store_dwordx2 v[66:67], v[4:5], off offset:1616
	v_cvt_pk_bf16_f32 v2, v10, v11
	v_cvt_pk_bf16_f32 v3, v12, v13
	v_pk_mul_f32 v[34:35], v[34:35], v[70:71] op_sel_hi:[1,0]
	v_pk_mul_f32 v[36:37], v[36:37], v[70:71] op_sel_hi:[1,0]
	v_cvt_pk_bf16_f32 v4, v26, v27
	v_cvt_pk_bf16_f32 v5, v28, v29
	global_store_dwordx2 v[66:67], v[2:3], off offset:1568
	global_store_dwordx2 v[66:67], v[4:5], off offset:1632
	v_cvt_pk_bf16_f32 v2, v14, v15
	v_cvt_pk_bf16_f32 v3, v16, v17
	v_pk_mul_f32 v[50:51], v[50:51], v[70:71] op_sel_hi:[1,0]
	v_pk_mul_f32 v[52:53], v[52:53], v[70:71] op_sel_hi:[1,0]
	v_pk_mul_f32 v[38:39], v[38:39], v[70:71] op_sel_hi:[1,0]
	v_pk_mul_f32 v[40:41], v[40:41], v[70:71] op_sel_hi:[1,0]
	v_cvt_pk_bf16_f32 v4, v30, v31
	v_cvt_pk_bf16_f32 v5, v32, v33
	global_store_dwordx2 v[66:67], v[2:3], off offset:1584
	global_store_dwordx2 v[66:67], v[4:5], off offset:1648
	v_cvt_pk_bf16_f32 v2, v34, v35
	v_cvt_pk_bf16_f32 v3, v36, v37
	v_pk_mul_f32 v[54:55], v[54:55], v[70:71] op_sel_hi:[1,0]
	v_pk_mul_f32 v[56:57], v[56:57], v[70:71] op_sel_hi:[1,0]
	v_pk_mul_f32 v[42:43], v[42:43], v[70:71] op_sel_hi:[1,0]
	v_pk_mul_f32 v[44:45], v[44:45], v[70:71] op_sel_hi:[1,0]
	v_cvt_pk_bf16_f32 v4, v50, v51
	v_cvt_pk_bf16_f32 v5, v52, v53
	global_store_dwordx2 v[66:67], v[2:3], off offset:1664
	global_store_dwordx2 v[66:67], v[4:5], off offset:1728
	v_cvt_pk_bf16_f32 v2, v38, v39
	v_cvt_pk_bf16_f32 v3, v40, v41
	v_pk_mul_f32 v[58:59], v[58:59], v[70:71] op_sel_hi:[1,0]
	v_pk_mul_f32 v[60:61], v[60:61], v[70:71] op_sel_hi:[1,0]
	v_pk_mul_f32 v[46:47], v[46:47], v[70:71] op_sel_hi:[1,0]
	v_pk_mul_f32 v[48:49], v[48:49], v[70:71] op_sel_hi:[1,0]
	v_cvt_pk_bf16_f32 v4, v54, v55
	v_cvt_pk_bf16_f32 v5, v56, v57
	global_store_dwordx2 v[66:67], v[2:3], off offset:1680
	global_store_dwordx2 v[66:67], v[4:5], off offset:1744
	v_cvt_pk_bf16_f32 v2, v42, v43
	v_cvt_pk_bf16_f32 v3, v44, v45
	v_pk_mul_f32 v[62:63], v[62:63], v[70:71] op_sel_hi:[1,0]
	v_pk_mul_f32 v[64:65], v[64:65], v[70:71] op_sel_hi:[1,0]
	v_cvt_pk_bf16_f32 v4, v58, v59
	v_cvt_pk_bf16_f32 v5, v60, v61
	global_store_dwordx2 v[66:67], v[2:3], off offset:1696
	global_store_dwordx2 v[66:67], v[4:5], off offset:1760
	v_cvt_pk_bf16_f32 v2, v46, v47
	v_cvt_pk_bf16_f32 v3, v48, v49
	v_cvt_pk_bf16_f32 v4, v62, v63
	v_cvt_pk_bf16_f32 v5, v64, v65
	global_store_dwordx2 v[66:67], v[2:3], off offset:1712
	global_store_dwordx2 v[66:67], v[4:5], off offset:1776
	s_branch .LBB0_965
